# attention tile loops: s_setprio 1 around the QK and PV MFMA bursts (per-segment raise, as the GEMM template does)
# baseline (speedup 1.0000x reference)
.LBB0_395:
	v_add_u32_e32 v147, s88, v149
	v_mov_b32_e32 v109, v180
	v_add_u32_e32 v180, v147, v151
	ds_read_b128 v[188:191], v180 offset:0
	v_mov_b32_e32 v110, v181
	v_add_u32_e32 v181, v147, v182
	ds_read_b128 v[218:221], v181 offset:0
	v_add_u32_e32 v187, v147, v183
	ds_read_b128 v[222:225], v187 offset:0
	s_waitcnt lgkmcnt(2)
	v_add_u32_e32 v147, v147, v184
	s_setprio 1
	v_mfma_f32_16x16x32_bf16 v[108:111], v[188:191], v[38:41], v[108:111]
	v_mfma_f32_16x16x32_bf16 v[112:115], v[188:191], v[54:57], v[112:115]
	ds_read_b128 v[188:191], v147 offset:0
	s_waitcnt lgkmcnt(2)
	v_mfma_f32_16x16x32_bf16 v[108:111], v[218:221], v[42:45], v[108:111]
	v_mfma_f32_16x16x32_bf16 v[112:115], v[218:221], v[58:61], v[112:115]
	ds_read_b128 v[218:221], v180 offset:0x1000
	s_waitcnt lgkmcnt(2)
	v_mfma_f32_16x16x32_bf16 v[108:111], v[222:225], v[46:49], v[108:111]
	ds_read_b128 v[226:229], v181 offset:0x1000
	s_waitcnt lgkmcnt(2)
	v_mfma_f32_16x16x32_bf16 v[222:225], v[222:225], v[62:65], v[112:115]
	v_mfma_f32_16x16x32_bf16 v[112:115], v[188:191], v[50:53], v[108:111]
	v_mfma_f32_16x16x32_bf16 v[108:111], v[188:191], v[66:69], v[222:225]
	ds_read_b128 v[188:191], v187 offset:0x1000
	s_waitcnt lgkmcnt(2)
	v_mfma_f32_16x16x32_bf16 v[116:119], v[218:221], v[38:41], v[116:119]
	v_mfma_f32_16x16x32_bf16 v[120:123], v[218:221], v[54:57], v[120:123]
	ds_read_b128 v[218:221], v147 offset:0x1000
	s_waitcnt lgkmcnt(2)
	v_mfma_f32_16x16x32_bf16 v[116:119], v[226:229], v[42:45], v[116:119]
	ds_read_b128 v[222:225], v180 offset:0x2000
	s_waitcnt lgkmcnt(2)
	v_mfma_f32_16x16x32_bf16 v[120:123], v[226:229], v[58:61], v[120:123]
	v_mfma_f32_16x16x32_bf16 v[116:119], v[188:191], v[46:49], v[116:119]
	ds_read_b128 v[226:229], v181 offset:0x2000
	s_waitcnt lgkmcnt(2)
	v_mfma_f32_16x16x32_bf16 v[188:191], v[188:191], v[62:65], v[120:123]
	v_mfma_f32_16x16x32_bf16 v[120:123], v[218:221], v[50:53], v[116:119]
	v_mfma_f32_16x16x32_bf16 v[116:119], v[218:221], v[66:69], v[188:191]
	ds_read_b128 v[188:191], v187 offset:0x2000
	s_waitcnt lgkmcnt(2)
	v_mfma_f32_16x16x32_bf16 v[124:127], v[222:225], v[38:41], v[124:127]
	ds_read_b128 v[218:221], v147 offset:0x2000
	s_waitcnt lgkmcnt(2)
	v_mfma_f32_16x16x32_bf16 v[132:135], v[222:225], v[54:57], v[132:135]
	v_mfma_f32_16x16x32_bf16 v[124:127], v[226:229], v[42:45], v[124:127]
	ds_read_b128 v[222:225], v180 offset:0x3000
	s_waitcnt lgkmcnt(2)
	v_mfma_f32_16x16x32_bf16 v[132:135], v[226:229], v[58:61], v[132:135]
	s_nop 1
	v_mfma_f32_16x16x32_bf16 v[124:127], v[188:191], v[46:49], v[124:127]
	ds_read_b128 v[226:229], v181 offset:0x3000
	s_waitcnt lgkmcnt(2)
	v_mfma_f32_16x16x32_bf16 v[188:191], v[188:191], v[62:65], v[132:135]
	v_mfma_f32_16x16x32_bf16 v[132:135], v[218:221], v[50:53], v[124:127]
	v_mfma_f32_16x16x32_bf16 v[124:127], v[218:221], v[66:69], v[188:191]
	ds_read_b128 v[188:191], v187 offset:0x3000
	s_waitcnt lgkmcnt(2)
	v_mfma_f32_16x16x32_bf16 v[128:131], v[222:225], v[38:41], v[128:131]
	ds_read_b128 v[218:221], v147 offset:0x3000
	s_waitcnt lgkmcnt(2)
	v_mfma_f32_16x16x32_bf16 v[136:139], v[222:225], v[54:57], v[136:139]
	v_mfma_f32_16x16x32_bf16 v[128:131], v[226:229], v[42:45], v[128:131]
	s_waitcnt lgkmcnt(1)
	v_mfma_f32_16x16x32_bf16 v[136:139], v[226:229], v[58:61], v[136:139]
	s_nop 1
	v_mfma_f32_16x16x32_bf16 v[128:131], v[188:191], v[46:49], v[128:131]
	s_waitcnt lgkmcnt(0)
	v_mfma_f32_16x16x32_bf16 v[188:191], v[188:191], v[62:65], v[136:139]
	v_and_b32_e32 v180, 64, v208
	v_xor_b32_e32 v147, 16, v208
	v_add_u32_e32 v180, 64, v180
	v_cmp_lt_i32_e32 vcc, v147, v180
	v_mfma_f32_16x16x32_bf16 v[136:139], v[218:221], v[50:53], v[128:131]
	s_mov_b64 s[0:1], 0
	v_cndmask_b32_e32 v147, v208, v147, vcc
	v_lshlrev_b32_e32 v181, 2, v147
	v_xor_b32_e32 v147, 32, v208
	v_cmp_lt_i32_e32 vcc, v147, v180
	v_mfma_f32_16x16x32_bf16 v[128:131], v[218:221], v[66:69], v[188:191]
	s_setprio 0
	s_mov_b64 s[54:55], 0
	v_cndmask_b32_e32 v147, v208, v147, vcc
	v_lshlrev_b32_e32 v187, 2, v147
	v_max3_f32 v147, v112, s30, v113
	v_max3_f32 v147, v147, v114, v115
	v_max3_f32 v147, v147, v120, v121
	v_max3_f32 v147, v147, v122, v123
	v_max3_f32 v147, v147, v132, v133
	v_max3_f32 v147, v147, v134, v135
	v_max3_f32 v147, v147, v136, v137
	v_max3_f32 v147, v147, v138, v139
	v_max3_f32 v180, v108, s30, v109
	v_max3_f32 v180, v180, v110, v111
	v_max3_f32 v180, v180, v116, v117
	v_max3_f32 v180, v180, v118, v119
	v_max3_f32 v180, v180, v124, v125
	v_max3_f32 v180, v180, v126, v127
	v_max3_f32 v180, v180, v128, v129
	v_max3_f32 v180, v180, v130, v131
	v_mov_b32_e32 v230, v147
	v_mov_b32_e32 v231, v180
	s_nop 1
	v_permlane16_swap_b32 v230, v147
	v_permlane16_swap_b32 v231, v180
	v_max_f32_e32 v147, v147, v230
	v_max_f32_e32 v180, v180, v231
	v_mov_b32_e32 v230, v147
	v_mov_b32_e32 v231, v180
	s_nop 1
	v_permlane32_swap_b32 v230, v147
	v_permlane32_swap_b32 v231, v180
	v_max_f32_e32 v147, v147, v230
	v_max_f32_e32 v180, v180, v231
	v_cmp_lt_f32_e64 s[56:57], s31, v147
	v_cmp_lt_f32_e32 vcc, s34, v147
	s_orn2_b64 s[54:55], vcc, s[52:53]
	s_and_b64 s[54:55], s[54:55], s[56:57]
	v_cmp_lt_f32_e64 s[56:57], s31, v180
	v_cmp_lt_f32_e32 vcc, s34, v180
	s_orn2_b64 s[0:1], vcc, s[48:49]
	s_and_b64 s[0:1], s[0:1], s[56:57]
	s_or_b64 s[56:57], s[54:55], s[0:1]
	s_cbranch_scc0 .LBB0_401
	v_cndmask_b32_e64 v188, 0, v180, s[0:1]
	v_cndmask_b32_e64 v147, 0, v147, s[54:55]
	v_exp_f32_e64 v180, -v188
	v_exp_f32_e64 v187, -v147
	s_and_b64 vcc, s[0:1], s[48:49]
	s_or_b64 s[0:1], s[48:49], s[0:1]
	v_cndmask_b32_e32 v181, 1.0, v180, vcc
	s_and_b64 vcc, s[54:55], s[52:53]
	v_cndmask_b32_e32 v180, 1.0, v187, vcc
	s_or_b64 s[54:55], s[52:53], s[54:55]
	v_pk_mul_f32 v[100:101], v[100:101], v[180:181] op_sel_hi:[1,0]
	v_pk_mul_f32 v[98:99], v[98:99], v[180:181] op_sel_hi:[1,0]
	v_pk_mul_f32 v[96:97], v[96:97], v[180:181] op_sel_hi:[1,0]
	v_pk_mul_f32 v[94:95], v[94:95], v[180:181] op_sel_hi:[1,0]
	v_pk_mul_f32 v[92:93], v[92:93], v[180:181] op_sel_hi:[1,0]
	v_pk_mul_f32 v[90:91], v[90:91], v[180:181] op_sel_hi:[1,0]
	v_pk_mul_f32 v[88:89], v[88:89], v[180:181] op_sel_hi:[1,0]
	v_pk_mul_f32 v[86:87], v[86:87], v[180:181] op_sel_hi:[1,0]
	v_pk_mul_f32 v[84:85], v[84:85], v[180:181] op_sel_hi:[1,0]
	v_pk_mul_f32 v[82:83], v[82:83], v[180:181] op_sel_hi:[1,0]
	v_pk_mul_f32 v[80:81], v[80:81], v[180:181] op_sel_hi:[1,0]
	v_pk_mul_f32 v[78:79], v[78:79], v[180:181] op_sel_hi:[1,0]
	v_pk_mul_f32 v[76:77], v[76:77], v[180:181] op_sel_hi:[1,0]
	v_pk_mul_f32 v[74:75], v[74:75], v[180:181] op_sel_hi:[1,0]
	v_pk_mul_f32 v[72:73], v[72:73], v[180:181] op_sel_hi:[1,0]
	v_pk_mul_f32 v[70:71], v[70:71], v[180:181] op_sel_hi:[1,0]
	v_pk_mul_f32 v[152:153], v[152:153], v[180:181]
	v_mov_b32_e32 v180, v181
	s_andn2_b64 s[52:53], s[52:53], exec
	s_and_b64 s[54:55], s[54:55], exec
	s_andn2_b64 s[48:49], s[48:49], exec
	s_and_b64 s[0:1], s[0:1], exec
	v_add_f32_e32 v146, v146, v147
	v_sub_f32_e32 v112, v112, v147
	v_sub_f32_e32 v113, v113, v147
	v_sub_f32_e32 v114, v114, v147
	v_sub_f32_e32 v115, v115, v147
	v_sub_f32_e32 v120, v120, v147
	v_sub_f32_e32 v121, v121, v147
	v_sub_f32_e32 v122, v122, v147
	v_sub_f32_e32 v123, v123, v147
	v_sub_f32_e32 v132, v132, v147
	v_sub_f32_e32 v133, v133, v147
	v_sub_f32_e32 v134, v134, v147
	v_sub_f32_e32 v135, v135, v147
	v_sub_f32_e32 v136, v136, v147
	v_sub_f32_e32 v137, v137, v147
	v_sub_f32_e32 v138, v138, v147
	v_sub_f32_e32 v139, v139, v147
	v_add_f32_e32 v2, v2, v188
	v_pk_mul_f32 v[36:37], v[36:37], v[180:181] op_sel_hi:[1,0]
	v_pk_mul_f32 v[34:35], v[34:35], v[180:181] op_sel_hi:[1,0]
	v_pk_mul_f32 v[32:33], v[32:33], v[180:181] op_sel_hi:[1,0]
	v_pk_mul_f32 v[30:31], v[30:31], v[180:181] op_sel_hi:[1,0]
	v_pk_mul_f32 v[28:29], v[28:29], v[180:181] op_sel_hi:[1,0]
	v_pk_mul_f32 v[26:27], v[26:27], v[180:181] op_sel_hi:[1,0]
	v_pk_mul_f32 v[20:21], v[20:21], v[180:181] op_sel_hi:[1,0]
	v_pk_mul_f32 v[18:19], v[18:19], v[180:181] op_sel_hi:[1,0]
	v_pk_mul_f32 v[24:25], v[24:25], v[180:181] op_sel_hi:[1,0]
	v_pk_mul_f32 v[22:23], v[22:23], v[180:181] op_sel_hi:[1,0]
	v_pk_mul_f32 v[16:17], v[16:17], v[180:181] op_sel_hi:[1,0]
	v_pk_mul_f32 v[14:15], v[14:15], v[180:181] op_sel_hi:[1,0]
	v_pk_mul_f32 v[12:13], v[12:13], v[180:181] op_sel_hi:[1,0]
	v_pk_mul_f32 v[10:11], v[10:11], v[180:181] op_sel_hi:[1,0]
	v_pk_mul_f32 v[8:9], v[8:9], v[180:181] op_sel_hi:[1,0]
	v_pk_mul_f32 v[6:7], v[6:7], v[180:181] op_sel_hi:[1,0]
	v_sub_f32_e32 v108, v108, v188
	v_sub_f32_e32 v109, v109, v188
	v_sub_f32_e32 v110, v110, v188
	v_sub_f32_e32 v111, v111, v188
	v_sub_f32_e32 v116, v116, v188
	v_sub_f32_e32 v117, v117, v188
	v_sub_f32_e32 v118, v118, v188
	v_sub_f32_e32 v119, v119, v188
	v_sub_f32_e32 v124, v124, v188
	v_sub_f32_e32 v125, v125, v188
	v_sub_f32_e32 v126, v126, v188
	v_sub_f32_e32 v127, v127, v188
	v_sub_f32_e32 v128, v128, v188
	v_sub_f32_e32 v129, v129, v188
	v_sub_f32_e32 v130, v130, v188
	v_sub_f32_e32 v131, v131, v188
	s_or_b64 s[52:53], s[52:53], s[54:55]
	s_or_b64 s[48:49], s[48:49], s[0:1]
.LBB0_401:
	v_add_u32_e32 v248, s88, v185
	ds_read_b64_tr_b16 v[232:233], v248 offset:0
	ds_read_b64_tr_b16 v[234:235], v248 offset:0x1000
	ds_read_b64_tr_b16 v[236:237], v248 offset:0x2000
	ds_read_b64_tr_b16 v[238:239], v248 offset:0x3000
	v_xor_b32_e32 v249, 32, v248
	ds_read_b64_tr_b16 v[240:241], v249 offset:0
	ds_read_b64_tr_b16 v[242:243], v249 offset:0x1000
	ds_read_b64_tr_b16 v[244:245], v249 offset:0x2000
	ds_read_b64_tr_b16 v[246:247], v249 offset:0x3000
	v_exp_f32_e32 v180, v112
	v_exp_f32_e32 v181, v108
	v_exp_f32_e32 v188, v113
	v_exp_f32_e32 v189, v109
	v_exp_f32_e32 v190, v114
	v_exp_f32_e32 v191, v110
	v_exp_f32_e32 v192, v115
	v_exp_f32_e32 v193, v111
	v_exp_f32_e32 v120, v120
	v_exp_f32_e32 v218, v121
	v_exp_f32_e32 v121, v116
	v_pk_add_f32 v[112:113], v[180:181], 0 op_sel_hi:[1,0]
	v_exp_f32_e32 v219, v117
	v_pk_add_f32 v[112:113], v[188:189], v[112:113]
	v_exp_f32_e32 v122, v122
	v_exp_f32_e32 v220, v123
	v_exp_f32_e32 v123, v118
	v_pk_add_f32 v[112:113], v[190:191], v[112:113]
	v_exp_f32_e32 v221, v119
	v_pk_add_f32 v[112:113], v[192:193], v[112:113]
	v_exp_f32_e32 v132, v132
	v_exp_f32_e32 v222, v133
	v_pk_add_f32 v[112:113], v[120:121], v[112:113]
	v_exp_f32_e32 v133, v124
	v_pk_add_f32 v[112:113], v[218:219], v[112:113]
	v_exp_f32_e32 v223, v125
	v_exp_f32_e32 v134, v134
	v_exp_f32_e32 v224, v135
	v_pk_add_f32 v[112:113], v[122:123], v[112:113]
	v_exp_f32_e32 v135, v126
	v_exp_f32_e32 v225, v127
	v_pk_add_f32 v[112:113], v[220:221], v[112:113]
	v_exp_f32_e32 v136, v136
	v_exp_f32_e32 v226, v137
	v_exp_f32_e32 v137, v128
	v_pk_add_f32 v[112:113], v[132:133], v[112:113]
	v_exp_f32_e32 v227, v129
	v_pk_add_f32 v[112:113], v[222:223], v[112:113]
	v_exp_f32_e32 v138, v138
	v_exp_f32_e32 v228, v139
	v_exp_f32_e32 v139, v130
	v_pk_add_f32 v[112:113], v[134:135], v[112:113]
	v_exp_f32_e32 v229, v131
	v_pk_add_f32 v[112:113], v[224:225], v[112:113]
	v_add_u32_e32 v147, s88, v185
	v_pk_add_f32 v[112:113], v[136:137], v[112:113]
	v_cvt_pk_bf16_f32 v108, v180, v188
	v_pk_add_f32 v[112:113], v[226:227], v[112:113]
	v_cvt_pk_bf16_f32 v110, v120, v218
	v_pk_add_f32 v[112:113], v[138:139], v[112:113]
	v_cvt_pk_bf16_f32 v120, v133, v223
	v_pk_add_f32 v[116:117], v[228:229], v[112:113]
	v_cvt_pk_bf16_f32 v112, v132, v222
	v_xor_b32_e32 v180, 32, v147
	v_cvt_pk_bf16_f32 v113, v134, v224
	v_cvt_pk_bf16_f32 v118, v121, v219
	v_cvt_pk_bf16_f32 v121, v135, v225
	v_cvt_pk_bf16_f32 v111, v122, v220
	v_cvt_pk_bf16_f32 v114, v136, v226
	v_cvt_pk_bf16_f32 v122, v137, v227
	v_cvt_pk_bf16_f32 v115, v138, v228
	v_cvt_pk_bf16_f32 v119, v123, v221
	v_cvt_pk_bf16_f32 v123, v139, v229
	v_pk_add_f32 v[152:153], v[152:153], v[116:117]
	v_cvt_pk_bf16_f32 v116, v181, v189
	v_xor_b32_e32 v180, 64, v147
	ds_read_b64_tr_b16 v[188:189], v180 offset:0
	v_cvt_pk_bf16_f32 v109, v190, v192
	v_cvt_pk_bf16_f32 v117, v191, v193
	ds_read_b64_tr_b16 v[190:191], v180 offset:0x1000
	ds_read_b64_tr_b16 v[218:219], v180 offset:0x2000
	ds_read_b64_tr_b16 v[220:221], v180 offset:0x3000
	v_xor_b32_e32 v180, 0x60, v147
	ds_read_b64_tr_b16 v[222:223], v180 offset:0
	ds_read_b64_tr_b16 v[224:225], v180 offset:0x1000
	ds_read_b64_tr_b16 v[226:227], v180 offset:0x2000
	ds_read_b64_tr_b16 v[228:229], v180 offset:0x3000
	s_waitcnt lgkmcnt(8)
	s_setprio 1
	v_mfma_f32_16x16x32_bf16 v[98:101], v[232:235], v[108:111], v[98:101]
	v_mfma_f32_16x16x32_bf16 v[34:37], v[232:235], v[116:119], v[34:37]
	v_mfma_f32_16x16x32_bf16 v[94:97], v[240:243], v[108:111], v[94:97]
	v_mfma_f32_16x16x32_bf16 v[30:33], v[240:243], v[116:119], v[30:33]
	v_mfma_f32_16x16x32_bf16 v[98:101], v[236:239], v[112:115], v[98:101]
	v_mfma_f32_16x16x32_bf16 v[34:37], v[236:239], v[120:123], v[34:37]
	v_mfma_f32_16x16x32_bf16 v[94:97], v[244:247], v[112:115], v[94:97]
	v_mfma_f32_16x16x32_bf16 v[30:33], v[244:247], v[120:123], v[30:33]
	v_xor_b32_e32 v132, 0x80, v147
	ds_read_b64_tr_b16 v[232:233], v132 offset:0
	ds_read_b64_tr_b16 v[234:235], v132 offset:0x1000
	ds_read_b64_tr_b16 v[236:237], v132 offset:0x2000
	ds_read_b64_tr_b16 v[238:239], v132 offset:0x3000
	v_xor_b32_e32 v180, 0xa0, v147
	ds_read_b64_tr_b16 v[240:241], v180 offset:0
	ds_read_b64_tr_b16 v[242:243], v180 offset:0x1000
	ds_read_b64_tr_b16 v[244:245], v180 offset:0x2000
	ds_read_b64_tr_b16 v[246:247], v180 offset:0x3000
	s_waitcnt lgkmcnt(8)
	v_mfma_f32_16x16x32_bf16 v[90:93], v[188:191], v[108:111], v[90:93]
	v_mfma_f32_16x16x32_bf16 v[26:29], v[188:191], v[116:119], v[26:29]
	v_mfma_f32_16x16x32_bf16 v[86:89], v[222:225], v[108:111], v[86:89]
	v_mfma_f32_16x16x32_bf16 v[18:21], v[222:225], v[116:119], v[18:21]
	v_mfma_f32_16x16x32_bf16 v[90:93], v[218:221], v[112:115], v[90:93]
	v_mfma_f32_16x16x32_bf16 v[26:29], v[218:221], v[120:123], v[26:29]
	v_mfma_f32_16x16x32_bf16 v[86:89], v[226:229], v[112:115], v[86:89]
	v_mfma_f32_16x16x32_bf16 v[18:21], v[226:229], v[120:123], v[18:21]
	v_xor_b32_e32 v180, 0xc0, v147
	ds_read_b64_tr_b16 v[188:189], v180 offset:0
	ds_read_b64_tr_b16 v[190:191], v180 offset:0x1000
	ds_read_b64_tr_b16 v[218:219], v180 offset:0x2000
	ds_read_b64_tr_b16 v[220:221], v180 offset:0x3000
	v_xor_b32_e32 v147, 0xe0, v147
	ds_read_b64_tr_b16 v[222:223], v147 offset:0
	ds_read_b64_tr_b16 v[224:225], v147 offset:0x1000
	ds_read_b64_tr_b16 v[226:227], v147 offset:0x2000
	ds_read_b64_tr_b16 v[228:229], v147 offset:0x3000
	s_waitcnt lgkmcnt(8)
	v_mfma_f32_16x16x32_bf16 v[82:85], v[232:235], v[108:111], v[82:85]
	v_mfma_f32_16x16x32_bf16 v[22:25], v[232:235], v[116:119], v[22:25]
	v_mfma_f32_16x16x32_bf16 v[78:81], v[240:243], v[108:111], v[78:81]
	v_mfma_f32_16x16x32_bf16 v[14:17], v[240:243], v[116:119], v[14:17]
	v_mfma_f32_16x16x32_bf16 v[82:85], v[236:239], v[112:115], v[82:85]
	v_mfma_f32_16x16x32_bf16 v[22:25], v[236:239], v[120:123], v[22:25]
	v_mfma_f32_16x16x32_bf16 v[78:81], v[244:247], v[112:115], v[78:81]
	v_mfma_f32_16x16x32_bf16 v[14:17], v[244:247], v[120:123], v[14:17]
	s_waitcnt lgkmcnt(0)
	v_mfma_f32_16x16x32_bf16 v[74:77], v[188:191], v[108:111], v[74:77]
	v_mfma_f32_16x16x32_bf16 v[10:13], v[188:191], v[116:119], v[10:13]
	v_mfma_f32_16x16x32_bf16 v[70:73], v[222:225], v[108:111], v[70:73]
	v_mfma_f32_16x16x32_bf16 v[6:9], v[222:225], v[116:119], v[6:9]
	v_mfma_f32_16x16x32_bf16 v[74:77], v[218:221], v[112:115], v[74:77]
	v_mfma_f32_16x16x32_bf16 v[10:13], v[218:221], v[120:123], v[10:13]
	v_mfma_f32_16x16x32_bf16 v[70:73], v[226:229], v[112:115], v[70:73]
	v_mfma_f32_16x16x32_bf16 v[6:9], v[226:229], v[120:123], v[6:9]
	s_setprio 0

.LBB0_413:
	v_add_u32_e32 v248, s67, v166
	ds_read_b64_tr_b16 v[232:233], v248 offset:0
	ds_read_b64_tr_b16 v[234:235], v248 offset:0x1000
	ds_read_b64_tr_b16 v[236:237], v248 offset:0x2000
	ds_read_b64_tr_b16 v[238:239], v248 offset:0x3000
	v_xor_b32_e32 v249, 32, v248
	ds_read_b64_tr_b16 v[240:241], v249 offset:0
	ds_read_b64_tr_b16 v[242:243], v249 offset:0x1000
	ds_read_b64_tr_b16 v[244:245], v249 offset:0x2000
	ds_read_b64_tr_b16 v[246:247], v249 offset:0x3000
	v_exp_f32_e32 v170, v110
	v_exp_f32_e32 v171, v106
	v_exp_f32_e32 v172, v111
	v_exp_f32_e32 v173, v107
	v_exp_f32_e32 v174, v112
	v_exp_f32_e32 v175, v108
	v_exp_f32_e32 v176, v113
	v_exp_f32_e32 v177, v109
	v_exp_f32_e32 v118, v118
	v_exp_f32_e32 v178, v119
	v_exp_f32_e32 v119, v114
	v_pk_add_f32 v[110:111], v[170:171], 0 op_sel_hi:[1,0]
	v_exp_f32_e32 v179, v115
	v_pk_add_f32 v[110:111], v[172:173], v[110:111]
	v_exp_f32_e32 v120, v120
	v_exp_f32_e32 v180, v121
	v_pk_add_f32 v[110:111], v[174:175], v[110:111]
	v_exp_f32_e32 v121, v116
	v_pk_add_f32 v[110:111], v[176:177], v[110:111]
	v_exp_f32_e32 v181, v117
	v_exp_f32_e32 v130, v130
	v_exp_f32_e32 v182, v131
	v_pk_add_f32 v[110:111], v[118:119], v[110:111]
	v_exp_f32_e32 v131, v122
	v_pk_add_f32 v[110:111], v[178:179], v[110:111]
	v_exp_f32_e32 v183, v123
	v_exp_f32_e32 v132, v132
	v_exp_f32_e32 v184, v133
	v_exp_f32_e32 v133, v124
	v_pk_add_f32 v[110:111], v[120:121], v[110:111]
	v_exp_f32_e32 v185, v125
	v_pk_add_f32 v[110:111], v[180:181], v[110:111]
	v_exp_f32_e32 v134, v134
	v_exp_f32_e32 v186, v135
	v_exp_f32_e32 v135, v126
	v_pk_add_f32 v[110:111], v[130:131], v[110:111]
	v_exp_f32_e32 v187, v127
	v_pk_add_f32 v[110:111], v[182:183], v[110:111]
	v_exp_f32_e32 v136, v136
	v_exp_f32_e32 v188, v137
	v_exp_f32_e32 v137, v128
	v_pk_add_f32 v[110:111], v[132:133], v[110:111]
	v_exp_f32_e32 v189, v129
	v_pk_add_f32 v[110:111], v[184:185], v[110:111]
	v_add_u32_e32 v158, s67, v166
	v_pk_add_f32 v[110:111], v[134:135], v[110:111]
	v_cvt_pk_bf16_f32 v108, v118, v178
	v_pk_add_f32 v[110:111], v[186:187], v[110:111]
	v_cvt_pk_bf16_f32 v118, v131, v183
	v_pk_add_f32 v[110:111], v[136:137], v[110:111]
	v_xor_b32_e32 v160, 32, v158
	v_pk_add_f32 v[114:115], v[188:189], v[110:111]
	v_cvt_pk_bf16_f32 v110, v130, v182
	v_cvt_pk_bf16_f32 v111, v132, v184
	v_cvt_pk_bf16_f32 v116, v119, v179
	v_cvt_pk_bf16_f32 v119, v133, v185
	v_cvt_pk_bf16_f32 v109, v120, v180
	v_cvt_pk_bf16_f32 v112, v134, v186
	v_cvt_pk_bf16_f32 v120, v135, v187
	v_cvt_pk_bf16_f32 v113, v136, v188
	v_cvt_pk_bf16_f32 v117, v121, v181
	v_cvt_pk_bf16_f32 v121, v137, v189
	v_cvt_pk_bf16_f32 v106, v170, v172
	v_pk_add_f32 v[144:145], v[144:145], v[114:115]
	v_cvt_pk_bf16_f32 v114, v171, v173
	v_xor_b32_e32 v160, 64, v158
	ds_read_b64_tr_b16 v[170:171], v160 offset:0
	ds_read_b64_tr_b16 v[172:173], v160 offset:0x1000
	v_cvt_pk_bf16_f32 v107, v174, v176
	v_cvt_pk_bf16_f32 v115, v175, v177
	ds_read_b64_tr_b16 v[174:175], v160 offset:0x2000
	ds_read_b64_tr_b16 v[176:177], v160 offset:0x3000
	v_xor_b32_e32 v160, 0x60, v158
	ds_read_b64_tr_b16 v[178:179], v160 offset:0
	ds_read_b64_tr_b16 v[180:181], v160 offset:0x1000
	ds_read_b64_tr_b16 v[182:183], v160 offset:0x2000
	ds_read_b64_tr_b16 v[184:185], v160 offset:0x3000
	s_waitcnt lgkmcnt(8)
	s_setprio 1
	v_mfma_f32_16x16x32_bf16 v[94:97], v[232:235], v[106:109], v[94:97]
	v_mfma_f32_16x16x32_bf16 v[42:45], v[232:235], v[114:117], v[42:45]
	v_mfma_f32_16x16x32_bf16 v[90:93], v[240:243], v[106:109], v[90:93]
	v_mfma_f32_16x16x32_bf16 v[26:29], v[240:243], v[114:117], v[26:29]
	v_mfma_f32_16x16x32_bf16 v[94:97], v[236:239], v[110:113], v[94:97]
	v_mfma_f32_16x16x32_bf16 v[42:45], v[236:239], v[118:121], v[42:45]
	v_mfma_f32_16x16x32_bf16 v[90:93], v[244:247], v[110:113], v[90:93]
	v_mfma_f32_16x16x32_bf16 v[26:29], v[244:247], v[118:121], v[26:29]
	v_xor_b32_e32 v130, 0x80, v158
	ds_read_b64_tr_b16 v[232:233], v130 offset:0
	ds_read_b64_tr_b16 v[234:235], v130 offset:0x1000
	ds_read_b64_tr_b16 v[236:237], v130 offset:0x2000
	ds_read_b64_tr_b16 v[238:239], v130 offset:0x3000
	v_xor_b32_e32 v160, 0xa0, v158
	ds_read_b64_tr_b16 v[240:241], v160 offset:0
	ds_read_b64_tr_b16 v[242:243], v160 offset:0x1000
	ds_read_b64_tr_b16 v[244:245], v160 offset:0x2000
	ds_read_b64_tr_b16 v[246:247], v160 offset:0x3000
	s_waitcnt lgkmcnt(8)
	v_mfma_f32_16x16x32_bf16 v[86:89], v[170:173], v[106:109], v[86:89]
	v_mfma_f32_16x16x32_bf16 v[22:25], v[170:173], v[114:117], v[22:25]
	v_mfma_f32_16x16x32_bf16 v[82:85], v[178:181], v[106:109], v[82:85]
	v_mfma_f32_16x16x32_bf16 v[18:21], v[178:181], v[114:117], v[18:21]
	v_mfma_f32_16x16x32_bf16 v[86:89], v[174:177], v[110:113], v[86:89]
	v_mfma_f32_16x16x32_bf16 v[22:25], v[174:177], v[118:121], v[22:25]
	v_mfma_f32_16x16x32_bf16 v[82:85], v[182:185], v[110:113], v[82:85]
	v_mfma_f32_16x16x32_bf16 v[18:21], v[182:185], v[118:121], v[18:21]
	v_xor_b32_e32 v160, 0xc0, v158
	ds_read_b64_tr_b16 v[170:171], v160 offset:0
	ds_read_b64_tr_b16 v[172:173], v160 offset:0x1000
	ds_read_b64_tr_b16 v[174:175], v160 offset:0x2000
	ds_read_b64_tr_b16 v[176:177], v160 offset:0x3000
	v_xor_b32_e32 v158, 0xe0, v158
	ds_read_b64_tr_b16 v[178:179], v158 offset:0
	ds_read_b64_tr_b16 v[180:181], v158 offset:0x1000
	ds_read_b64_tr_b16 v[182:183], v158 offset:0x2000
	ds_read_b64_tr_b16 v[184:185], v158 offset:0x3000
	s_waitcnt lgkmcnt(8)
	v_mfma_f32_16x16x32_bf16 v[78:81], v[232:235], v[106:109], v[78:81]
	v_mfma_f32_16x16x32_bf16 v[14:17], v[232:235], v[114:117], v[14:17]
	v_mfma_f32_16x16x32_bf16 v[74:77], v[240:243], v[106:109], v[74:77]
	v_mfma_f32_16x16x32_bf16 v[2:5], v[240:243], v[114:117], v[2:5]
	v_mfma_f32_16x16x32_bf16 v[78:81], v[236:239], v[110:113], v[78:81]
	v_mfma_f32_16x16x32_bf16 v[14:17], v[236:239], v[118:121], v[14:17]
	v_mfma_f32_16x16x32_bf16 v[74:77], v[244:247], v[110:113], v[74:77]
	v_mfma_f32_16x16x32_bf16 v[2:5], v[244:247], v[118:121], v[2:5]
	s_waitcnt lgkmcnt(0)
	v_mfma_f32_16x16x32_bf16 v[70:73], v[170:173], v[106:109], v[70:73]
	v_mfma_f32_16x16x32_bf16 v[10:13], v[170:173], v[114:117], v[10:13]
	v_mfma_f32_16x16x32_bf16 v[66:69], v[178:181], v[106:109], v[66:69]
	v_mfma_f32_16x16x32_bf16 v[6:9], v[178:181], v[114:117], v[6:9]
	v_mfma_f32_16x16x32_bf16 v[70:73], v[174:177], v[110:113], v[70:73]
	v_mfma_f32_16x16x32_bf16 v[10:13], v[174:177], v[118:121], v[10:13]
	v_mfma_f32_16x16x32_bf16 v[66:69], v[182:185], v[110:113], v[66:69]
	v_mfma_f32_16x16x32_bf16 v[6:9], v[182:185], v[118:121], v[6:9]
	s_setprio 0

.LBB0_420:
	v_add_u32_e32 v158, s67, v161
	v_add_u32_e32 v160, v158, v162
	ds_read_b128 v[170:173], v160 offset:0
	v_add_u32_e32 v169, v158, v163
	ds_read_b128 v[174:177], v169 offset:0
	v_add_u32_e32 v186, v158, v164
	ds_read_b128 v[178:181], v186 offset:0
	s_waitcnt lgkmcnt(2)
	v_add_u32_e32 v158, v158, v165
	s_setprio 1
	v_mfma_f32_16x16x32_bf16 v[106:109], v[170:173], v[30:33], v[106:109]
	v_mfma_f32_16x16x32_bf16 v[110:113], v[170:173], v[50:53], v[110:113]
	ds_read_b128 v[170:173], v158 offset:0
	s_waitcnt lgkmcnt(2)
	v_mfma_f32_16x16x32_bf16 v[106:109], v[174:177], v[34:37], v[106:109]
	v_mfma_f32_16x16x32_bf16 v[110:113], v[174:177], v[54:57], v[110:113]
	ds_read_b128 v[174:177], v160 offset:0x1000
	s_waitcnt lgkmcnt(2)
	v_mfma_f32_16x16x32_bf16 v[106:109], v[178:181], v[38:41], v[106:109]
	ds_read_b128 v[182:185], v169 offset:0x1000
	s_waitcnt lgkmcnt(2)
	v_mfma_f32_16x16x32_bf16 v[178:181], v[178:181], v[58:61], v[110:113]
	v_mfma_f32_16x16x32_bf16 v[110:113], v[170:173], v[46:49], v[106:109]
	v_mfma_f32_16x16x32_bf16 v[106:109], v[170:173], v[62:65], v[178:181]
	ds_read_b128 v[170:173], v186 offset:0x1000
	s_waitcnt lgkmcnt(2)
	v_mfma_f32_16x16x32_bf16 v[114:117], v[174:177], v[30:33], v[114:117]
	v_mfma_f32_16x16x32_bf16 v[118:121], v[174:177], v[50:53], v[118:121]
	ds_read_b128 v[174:177], v158 offset:0x1000
	s_waitcnt lgkmcnt(2)
	v_mfma_f32_16x16x32_bf16 v[114:117], v[182:185], v[34:37], v[114:117]
	ds_read_b128 v[178:181], v160 offset:0x2000
	s_waitcnt lgkmcnt(2)
	v_mfma_f32_16x16x32_bf16 v[118:121], v[182:185], v[54:57], v[118:121]
	v_mfma_f32_16x16x32_bf16 v[114:117], v[170:173], v[38:41], v[114:117]
	ds_read_b128 v[182:185], v169 offset:0x2000
	s_waitcnt lgkmcnt(2)
	v_mfma_f32_16x16x32_bf16 v[170:173], v[170:173], v[58:61], v[118:121]
	v_mfma_f32_16x16x32_bf16 v[118:121], v[174:177], v[46:49], v[114:117]
	v_mfma_f32_16x16x32_bf16 v[114:117], v[174:177], v[62:65], v[170:173]
	ds_read_b128 v[170:173], v186 offset:0x2000
	s_waitcnt lgkmcnt(2)
	v_mfma_f32_16x16x32_bf16 v[122:125], v[178:181], v[30:33], v[122:125]
	ds_read_b128 v[174:177], v158 offset:0x2000
	s_waitcnt lgkmcnt(2)
	v_mfma_f32_16x16x32_bf16 v[130:133], v[178:181], v[50:53], v[130:133]
	v_mfma_f32_16x16x32_bf16 v[122:125], v[182:185], v[34:37], v[122:125]
	ds_read_b128 v[178:181], v160 offset:0x3000
	s_waitcnt lgkmcnt(2)
	v_mfma_f32_16x16x32_bf16 v[130:133], v[182:185], v[54:57], v[130:133]
	s_nop 1
	v_mfma_f32_16x16x32_bf16 v[122:125], v[170:173], v[38:41], v[122:125]
	ds_read_b128 v[182:185], v169 offset:0x3000
	s_waitcnt lgkmcnt(2)
	v_mfma_f32_16x16x32_bf16 v[170:173], v[170:173], v[58:61], v[130:133]
	v_mfma_f32_16x16x32_bf16 v[130:133], v[174:177], v[46:49], v[122:125]
	v_mfma_f32_16x16x32_bf16 v[122:125], v[174:177], v[62:65], v[170:173]
	ds_read_b128 v[170:173], v186 offset:0x3000
	s_waitcnt lgkmcnt(2)
	v_mfma_f32_16x16x32_bf16 v[126:129], v[178:181], v[30:33], v[126:129]
	ds_read_b128 v[174:177], v158 offset:0x3000
	s_waitcnt lgkmcnt(2)
	v_mfma_f32_16x16x32_bf16 v[134:137], v[178:181], v[50:53], v[134:137]
	v_mfma_f32_16x16x32_bf16 v[126:129], v[182:185], v[34:37], v[126:129]
	s_waitcnt lgkmcnt(1)
	v_mfma_f32_16x16x32_bf16 v[134:137], v[182:185], v[54:57], v[134:137]
	s_nop 1
	v_mfma_f32_16x16x32_bf16 v[126:129], v[170:173], v[38:41], v[126:129]
	s_waitcnt lgkmcnt(0)
	v_mfma_f32_16x16x32_bf16 v[170:173], v[170:173], v[58:61], v[134:137]
	v_and_b32_e32 v160, 64, v208
	v_xor_b32_e32 v158, 16, v208
	v_add_u32_e32 v160, 64, v160
	v_cmp_lt_i32_e32 vcc, v158, v160
	v_mfma_f32_16x16x32_bf16 v[134:137], v[174:177], v[46:49], v[126:129]
	s_mov_b64 s[48:49], 0
	v_cndmask_b32_e32 v158, v208, v158, vcc
	v_lshlrev_b32_e32 v169, 2, v158
	v_xor_b32_e32 v158, 32, v208
	v_cmp_lt_i32_e32 vcc, v158, v160
	v_mfma_f32_16x16x32_bf16 v[126:129], v[174:177], v[62:65], v[170:173]
	s_setprio 0
	s_mov_b64 s[52:53], 0
	v_cndmask_b32_e32 v158, v208, v158, vcc
	s_nop 0
	v_lshlrev_b32_e32 v170, 2, v158
	v_max3_f32 v158, v110, s30, v111
	v_max3_f32 v158, v158, v112, v113
	v_max3_f32 v158, v158, v118, v119
	v_max3_f32 v158, v158, v120, v121
	v_max3_f32 v158, v158, v130, v131
	v_max3_f32 v158, v158, v132, v133
	v_max3_f32 v158, v158, v134, v135
	v_max3_f32 v158, v158, v136, v137
	v_max3_f32 v160, v106, s30, v107
	v_max3_f32 v160, v160, v108, v109
	v_max3_f32 v160, v160, v114, v115
	v_max3_f32 v160, v160, v116, v117
	v_max3_f32 v160, v160, v122, v123
	v_max3_f32 v160, v160, v124, v125
	v_max3_f32 v160, v160, v126, v127
	v_max3_f32 v160, v160, v128, v129
	v_mov_b32_e32 v230, v158
	v_mov_b32_e32 v231, v160
	s_nop 1
	v_permlane16_swap_b32 v230, v158
	v_permlane16_swap_b32 v231, v160
	v_max_f32_e32 v158, v158, v230
	v_max_f32_e32 v160, v160, v231
	v_mov_b32_e32 v230, v158
	v_mov_b32_e32 v231, v160
	s_nop 1
	v_permlane32_swap_b32 v230, v158
	v_permlane32_swap_b32 v231, v160
	v_max_f32_e32 v158, v158, v230
	v_max_f32_e32 v160, v160, v231
	v_cmp_lt_f32_e64 s[54:55], s31, v158
	v_cmp_lt_f32_e32 vcc, s34, v158
	s_orn2_b64 s[52:53], vcc, s[46:47]
	s_and_b64 s[52:53], s[52:53], s[54:55]
	v_cmp_lt_f32_e64 s[54:55], s31, v160
	v_cmp_lt_f32_e32 vcc, s34, v160
	s_orn2_b64 s[48:49], vcc, s[44:45]
	s_and_b64 s[48:49], s[48:49], s[54:55]
	s_or_b64 s[54:55], s[52:53], s[48:49]
	s_cbranch_scc0 .LBB0_413
	v_cndmask_b32_e64 v160, 0, v160, s[48:49]
	v_cndmask_b32_e64 v158, 0, v158, s[52:53]
	v_exp_f32_e64 v170, -v160
	v_exp_f32_e64 v169, -v158
	s_and_b64 vcc, s[48:49], s[44:45]
	s_or_b64 s[48:49], s[44:45], s[48:49]
	v_cndmask_b32_e32 v171, 1.0, v170, vcc
	s_and_b64 vcc, s[52:53], s[46:47]
	s_or_b64 s[52:53], s[46:47], s[52:53]
	v_add_f32_e32 v167, v167, v158
	v_sub_f32_e32 v110, v110, v158
	v_sub_f32_e32 v111, v111, v158
	v_sub_f32_e32 v112, v112, v158
	v_sub_f32_e32 v113, v113, v158
	v_sub_f32_e32 v118, v118, v158
	v_sub_f32_e32 v119, v119, v158
	v_sub_f32_e32 v120, v120, v158
	v_sub_f32_e32 v121, v121, v158
	v_sub_f32_e32 v130, v130, v158
	v_sub_f32_e32 v131, v131, v158
	v_sub_f32_e32 v132, v132, v158
	v_sub_f32_e32 v133, v133, v158
	v_sub_f32_e32 v134, v134, v158
	v_sub_f32_e32 v135, v135, v158
	v_sub_f32_e32 v136, v136, v158
	v_sub_f32_e32 v137, v137, v158
	v_cndmask_b32_e32 v170, 1.0, v169, vcc
	v_mov_b32_e32 v158, v171
	s_andn2_b64 s[46:47], s[46:47], exec
	s_and_b64 s[52:53], s[52:53], exec
	s_andn2_b64 s[44:45], s[44:45], exec
	s_and_b64 s[48:49], s[48:49], exec
	v_pk_mul_f32 v[96:97], v[96:97], v[170:171] op_sel_hi:[1,0]
	v_pk_mul_f32 v[94:95], v[94:95], v[170:171] op_sel_hi:[1,0]
	v_pk_mul_f32 v[92:93], v[92:93], v[170:171] op_sel_hi:[1,0]
	v_pk_mul_f32 v[90:91], v[90:91], v[170:171] op_sel_hi:[1,0]
	v_pk_mul_f32 v[88:89], v[88:89], v[170:171] op_sel_hi:[1,0]
	v_pk_mul_f32 v[86:87], v[86:87], v[170:171] op_sel_hi:[1,0]
	v_pk_mul_f32 v[84:85], v[84:85], v[170:171] op_sel_hi:[1,0]
	v_pk_mul_f32 v[82:83], v[82:83], v[170:171] op_sel_hi:[1,0]
	v_pk_mul_f32 v[80:81], v[80:81], v[170:171] op_sel_hi:[1,0]
	v_pk_mul_f32 v[78:79], v[78:79], v[170:171] op_sel_hi:[1,0]
	v_pk_mul_f32 v[76:77], v[76:77], v[170:171] op_sel_hi:[1,0]
	v_pk_mul_f32 v[74:75], v[74:75], v[170:171] op_sel_hi:[1,0]
	v_pk_mul_f32 v[72:73], v[72:73], v[170:171] op_sel_hi:[1,0]
	v_pk_mul_f32 v[70:71], v[70:71], v[170:171] op_sel_hi:[1,0]
	v_pk_mul_f32 v[68:69], v[68:69], v[170:171] op_sel_hi:[1,0]
	v_pk_mul_f32 v[66:67], v[66:67], v[170:171] op_sel_hi:[1,0]
	v_add_f32_e32 v168, v168, v160
	v_pk_mul_f32 v[144:145], v[144:145], v[170:171]
	v_pk_mul_f32 v[44:45], v[44:45], v[158:159] op_sel_hi:[1,0]
	v_pk_mul_f32 v[42:43], v[42:43], v[158:159] op_sel_hi:[1,0]
	v_pk_mul_f32 v[28:29], v[28:29], v[158:159] op_sel_hi:[1,0]
	v_pk_mul_f32 v[26:27], v[26:27], v[158:159] op_sel_hi:[1,0]
	v_pk_mul_f32 v[24:25], v[24:25], v[158:159] op_sel_hi:[1,0]
	v_pk_mul_f32 v[22:23], v[22:23], v[158:159] op_sel_hi:[1,0]
	v_pk_mul_f32 v[20:21], v[20:21], v[158:159] op_sel_hi:[1,0]
	v_pk_mul_f32 v[18:19], v[18:19], v[158:159] op_sel_hi:[1,0]
	v_pk_mul_f32 v[16:17], v[16:17], v[158:159] op_sel_hi:[1,0]
	v_pk_mul_f32 v[14:15], v[14:15], v[158:159] op_sel_hi:[1,0]
	v_pk_mul_f32 v[4:5], v[4:5], v[158:159] op_sel_hi:[1,0]
	v_pk_mul_f32 v[2:3], v[2:3], v[158:159] op_sel_hi:[1,0]
	v_pk_mul_f32 v[12:13], v[12:13], v[158:159] op_sel_hi:[1,0]
	v_pk_mul_f32 v[10:11], v[10:11], v[158:159] op_sel_hi:[1,0]
	v_pk_mul_f32 v[8:9], v[8:9], v[158:159] op_sel_hi:[1,0]
	v_pk_mul_f32 v[6:7], v[6:7], v[158:159] op_sel_hi:[1,0]
	v_sub_f32_e32 v106, v106, v160
	v_sub_f32_e32 v107, v107, v160
	v_sub_f32_e32 v108, v108, v160
	v_sub_f32_e32 v109, v109, v160
	v_sub_f32_e32 v114, v114, v160
	v_sub_f32_e32 v115, v115, v160
	v_sub_f32_e32 v116, v116, v160
	v_sub_f32_e32 v117, v117, v160
	v_sub_f32_e32 v122, v122, v160
	v_sub_f32_e32 v123, v123, v160
	v_sub_f32_e32 v124, v124, v160
	v_sub_f32_e32 v125, v125, v160
	v_sub_f32_e32 v126, v126, v160
	v_sub_f32_e32 v127, v127, v160
	v_sub_f32_e32 v128, v128, v160
	v_sub_f32_e32 v129, v129, v160
	s_or_b64 s[46:47], s[46:47], s[52:53]
	s_or_b64 s[44:45], s[44:45], s[48:49]
	s_branch .LBB0_413
